# v5 + P3 row loop: cache-line touch loads for the later c_kv / misc loads of the row
# baseline (speedup 1.0000x reference)
.LBB0_734:
	v_readlane_b32 s16, v254, 3
	v_readlane_b32 s30, v254, 17
	v_readlane_b32 s31, v254, 18
	v_mov_b32_e32 v66, 0
	v_mov_b32_e32 v67, 0
	v_lshl_add_u64 v[46:47], s[30:31], 0, v[38:39]
	global_load_dwordx4 v[56:59], v[46:47], off
	global_load_dwordx4 v[60:63], v[46:47], off offset:-1024
	global_load_dword v94, v[46:47], off offset:1024
	v_lshl_add_u64 v[96:97], s[30:31], 0, v[40:41]
	global_load_dword v94, v[96:97], off offset:-256
	global_load_dword v94, v[96:97], off
	global_load_dword v94, v[96:97], off offset:128
	s_waitcnt vmcnt(25)
	v_lshl_add_u64 v[64:65], s[30:31], 0, v[34:35]
	v_add_co_u32_e64 v64, s[6:7], s33, v64
	v_lshl_add_u64 v[68:69], s[30:31], 0, v[32:33]
	s_nop 0
	v_addc_co_u32_e64 v65, s[6:7], 0, v65, s[6:7]
	v_add_co_u32_e64 v68, s[6:7], s35, v68
	s_waitcnt vmcnt(24)
	v_mov_b32_e32 v70, 0
	v_addc_co_u32_e64 v69, s[6:7], 0, v69, s[6:7]
	v_readlane_b32 s17, v254, 4
	v_readlane_b32 s18, v254, 5
	v_readlane_b32 s19, v254, 6
	v_readlane_b32 s20, v254, 7
	v_readlane_b32 s21, v254, 8
	v_readlane_b32 s22, v254, 9
	v_readlane_b32 s23, v254, 10
	v_readlane_b32 s24, v254, 11
	v_readlane_b32 s25, v254, 12
	v_readlane_b32 s26, v254, 13
	v_readlane_b32 s27, v254, 14
	v_readlane_b32 s28, v254, 15
	v_readlane_b32 s29, v254, 16
	s_waitcnt vmcnt(5)
	v_lshlrev_b32_e32 v72, 16, v58
	s_waitcnt vmcnt(4)
	v_lshlrev_b32_e32 v74, 16, v60
	v_and_b32_e32 v75, 0xffff0000, v60
	v_lshlrev_b32_e32 v60, 16, v61
	v_and_b32_e32 v61, 0xffff0000, v61
	v_lshlrev_b32_e32 v77, 16, v63
	v_lshlrev_b32_e32 v76, 16, v62
	v_and_b32_e32 v63, 0xffff0000, v63
	v_and_b32_e32 v62, 0xffff0000, v62
	v_mul_f32_e32 v80, v74, v74
	v_mul_f32_e32 v82, v60, v60
	v_lshlrev_b32_e32 v78, 16, v56
	v_and_b32_e32 v79, 0xffff0000, v56
	v_lshlrev_b32_e32 v56, 16, v57
	v_pk_mul_f32 v[84:85], v[62:63], v[62:63]
	v_pk_fma_f32 v[80:81], v[74:75], v[74:75], v[80:81] op_sel_hi:[1,1,0]
	v_pk_fma_f32 v[82:83], v[60:61], v[60:61], v[82:83] op_sel_hi:[1,1,0]
	v_and_b32_e32 v57, 0xffff0000, v57
	v_mul_f32_e32 v86, v78, v78
	v_mul_f32_e32 v88, v56, v56
	v_mov_b32_e32 v90, v72
	v_pk_fma_f32 v[84:85], v[76:77], v[76:77], v[84:85]
	v_mov_b32_e32 v73, v81
	v_mov_b32_e32 v91, v83
	v_and_b32_e32 v45, 0xffff0000, v58
	v_lshlrev_b32_e32 v58, 16, v59
	v_and_b32_e32 v59, 0xffff0000, v59
	v_pk_fma_f32 v[86:87], v[78:79], v[78:79], v[86:87] op_sel_hi:[1,1,0]
	v_pk_fma_f32 v[88:89], v[56:57], v[56:57], v[88:89] op_sel_hi:[1,1,0]
	v_pk_add_f32 v[84:85], v[84:85], v[84:85] op_sel_hi:[0,1]
	v_pk_add_f32 v[80:81], v[80:81], v[82:83]
	v_pk_mul_f32 v[82:83], v[72:73], v[90:91]
	v_mul_f32_e32 v86, v58, v58
	v_mul_f32_e32 v88, v59, v59
	v_mul_f32_e32 v84, v45, v45
	v_mov_b32_e32 v83, v81
	v_pk_add_f32 v[86:87], v[86:87], v[88:89]
	v_pk_add_f32 v[80:81], v[82:83], v[84:85]
	v_mov_b32_e32 v73, v45
	v_pk_add_f32 v[80:81], v[80:81], v[86:87]
	v_mov_b32_e32 v92, v76
	v_add_f32_e32 v55, v80, v81
	v_mov_b32_e32 v71, v55
	v_mov_b32_e32 v93, v62
	v_mov_b32_e32 v62, v77
	v_mov_b32_dpp v71, v71 row_ror:8 row_mask:0xf bank_mask:0xf
	v_add_f32_e32 v55, v55, v71
	v_mov_b32_e32 v71, v55
	s_nop 1
	v_mov_b32_dpp v71, v71 row_ror:4 row_mask:0xf bank_mask:0xf
	v_add_f32_e32 v55, v55, v71
	v_mov_b32_e32 v71, v55
	s_nop 1
	v_mov_b32_dpp v71, v71 row_ror:2 row_mask:0xf bank_mask:0xf
	v_add_f32_e32 v55, v55, v71
	v_mov_b32_e32 v71, v55
	s_nop 1
	v_mov_b32_dpp v71, v71 row_ror:1 row_mask:0xf bank_mask:0xf
	v_add_f32_e32 v55, v55, v71
	s_nop 0
	v_readlane_b32 s8, v55, 16
	v_readlane_b32 s9, v55, 48
	v_readlane_b32 s6, v55, 0
	v_readlane_b32 s7, v55, 32
	v_mov_b32_e32 v80, s8
	v_mov_b32_e32 v81, s9
	v_pk_add_f32 v[80:81], s[6:7], v[80:81]
	s_nop 0
	v_add_f32_e32 v55, v80, v81
	v_fmamk_f32 v55, v55, 0x3a800000, v42
	v_mul_f32_e32 v71, 0x4b800000, v55
	v_cmp_gt_f32_e64 s[6:7], s11, v55
	s_nop 1
	v_cndmask_b32_e64 v55, v55, v71, s[6:7]
	v_rsq_f32_e32 v55, v55
	s_nop 0
	v_mul_f32_e32 v45, 0x45800000, v55
	v_cndmask_b32_e64 v76, v55, v45, s[6:7]
	v_pk_mul_f32 v[74:75], v[76:77], v[74:75] op_sel_hi:[0,1]
	v_pk_mul_f32 v[74:75], v[14:15], v[74:75]
	v_pk_mul_f32 v[80:81], v[76:77], v[92:93] op_sel_hi:[0,1]
	v_med3_f32 v45, v74, s34, v51
	v_med3_f32 v55, v75, s34, v51
	v_cvt_pk_fp8_f32 v66, v45, v55
	v_pk_mul_f32 v[60:61], v[76:77], v[60:61] op_sel_hi:[0,1]
	v_pk_mul_f32 v[62:63], v[76:77], v[62:63] op_sel_hi:[0,1]
	v_pk_mul_f32 v[78:79], v[76:77], v[78:79] op_sel_hi:[0,1]
	v_pk_mul_f32 v[56:57], v[76:77], v[56:57] op_sel_hi:[0,1]
	v_pk_mul_f32 v[72:73], v[72:73], v[76:77] op_sel_hi:[1,0]
	v_pk_mul_f32 v[58:59], v[58:59], v[76:77] op_sel_hi:[1,0]
	v_pk_mul_f32 v[76:77], v[6:7], v[80:81]
	v_pk_mul_f32 v[60:61], v[16:17], v[60:61]
	v_pk_mul_f32 v[62:63], v[8:9], v[62:63]
	v_pk_mul_f32 v[80:81], v[24:25], v[56:57]
	v_pk_mul_f32 v[78:79], v[22:23], v[78:79]
	v_pk_mul_f32 v[82:83], v[20:21], v[58:59]
	v_cvt_pk_bf16_f32 v56, v74, v75
	v_cvt_pk_bf16_f32 v58, v76, v77
	v_med3_f32 v75, v76, s34, v51
	v_med3_f32 v76, v77, s34, v51
	v_pk_mul_f32 v[72:73], v[18:19], v[72:73]
	v_cvt_pk_bf16_f32 v57, v60, v61
	v_cvt_pk_bf16_f32 v59, v62, v63
	v_med3_f32 v71, v60, s34, v51
	v_med3_f32 v74, v61, s34, v51
	v_cvt_pk_fp8_f32 v67, v75, v76
	v_med3_f32 v45, v78, s34, v51
	v_med3_f32 v55, v79, s34, v51
	v_cvt_pk_fp8_f32 v66, v71, v74 op_sel:[0,0,1]
	global_store_dwordx4 v[64:65], v[56:59], off
	v_cvt_pk_fp8_f32 v70, v45, v55
	v_med3_f32 v55, v72, s34, v51
	v_med3_f32 v56, v73, s34, v51
	v_mov_b32_e32 v71, 0
	v_cvt_pk_fp8_f32 v71, v55, v56
	v_med3_f32 v62, v62, s34, v51
	v_med3_f32 v63, v63, s34, v51
	v_cvt_pk_fp8_f32 v67, v62, v63 op_sel:[0,0,1]
	v_med3_f32 v62, v80, s34, v51
	v_med3_f32 v45, v81, s34, v51
	v_cvt_pk_fp8_f32 v70, v62, v45 op_sel:[0,0,1]
	v_med3_f32 v45, v82, s34, v51
	v_med3_f32 v55, v83, s34, v51
	v_cvt_pk_fp8_f32 v71, v45, v55 op_sel:[0,0,1]
	v_cvt_pk_bf16_f32 v60, v78, v79
	v_cvt_pk_bf16_f32 v61, v80, v81
	v_cvt_pk_bf16_f32 v62, v72, v73
	v_cvt_pk_bf16_f32 v63, v82, v83
	global_store_dwordx2 v[68:69], v[66:67], off
	global_store_dwordx4 v[64:65], v[60:63], off offset:1024
	global_store_dwordx2 v[68:69], v[70:71], off offset:512
	global_load_dwordx4 v[56:59], v[46:47], off offset:1024
	v_lshl_add_u64 v[46:47], s[30:31], 0, v[40:41]
	global_load_dword v45, v[46:47], off offset:-256
	v_lshl_add_u64 v[60:61], s[30:31], 0, v[36:37]
	s_waitcnt vmcnt(1)
	v_lshlrev_b32_e32 v63, 16, v57
	v_lshlrev_b32_e32 v62, 16, v56
	v_and_b32_e32 v57, 0xffff0000, v57
	v_and_b32_e32 v56, 0xffff0000, v56
	s_waitcnt vmcnt(0)
	v_mov_b32_e32 v55, v45
	v_lshlrev_b32_e32 v65, 16, v59
	v_lshlrev_b32_e32 v64, 16, v58
	v_and_b32_e32 v59, 0xffff0000, v59
	v_and_b32_e32 v58, 0xffff0000, v58
	v_pk_mul_f32 v[66:67], v[56:57], v[56:57]
	v_mov_b32_dpp v55, v55 row_ror:8 row_mask:0xf bank_mask:0xf
	v_pk_mul_f32 v[68:69], v[58:59], v[58:59]
	v_mov_b32_e32 v70, v62
	v_mov_b32_e32 v71, v56
	v_mov_b32_e32 v56, v63
	v_pk_fma_f32 v[62:63], v[62:63], v[62:63], v[66:67]
	v_add_f32_e32 v55, v45, v55
	v_pk_fma_f32 v[66:67], v[64:65], v[64:65], v[68:69]
	v_add_f32_e32 v62, v62, v63
	v_mov_b32_e32 v63, v55
	v_add_f32_e32 v62, v66, v62
	v_add_f32_e32 v62, v67, v62
	v_mov_b32_dpp v63, v63 row_ror:4 row_mask:0xf bank_mask:0xf
	v_add_f32_e32 v55, v55, v63
	v_mov_b32_e32 v72, v64
	v_mov_b32_e32 v63, v62
	v_mov_b32_e32 v64, v55
	v_mov_b32_e32 v73, v58
	v_mov_b32_dpp v63, v63 row_ror:8 row_mask:0xf bank_mask:0xf
	v_mov_b32_dpp v64, v64 row_ror:2 row_mask:0xf bank_mask:0xf
	v_add_f32_e32 v62, v62, v63
	v_add_f32_e32 v55, v55, v64
	v_mov_b32_e32 v63, v62
	v_mov_b32_e32 v64, v55
	v_mov_b32_e32 v58, v65
	v_mov_b32_dpp v63, v63 row_ror:4 row_mask:0xf bank_mask:0xf
	v_mov_b32_dpp v64, v64 row_ror:1 row_mask:0xf bank_mask:0xf
	v_add_f32_e32 v66, v62, v63
	v_add_f32_e32 v55, v55, v64
	v_mov_b32_e32 v64, v66
	v_readlane_b32 s8, v55, 16
	v_readlane_b32 s9, v55, 48
	v_readlane_b32 s6, v55, 0
	v_readlane_b32 s7, v55, 32
	v_mov_b32_dpp v64, v64 row_ror:2 row_mask:0xf bank_mask:0xf
	v_mov_b32_e32 v62, s8
	v_mov_b32_e32 v63, s9
	v_add_f32_e32 v55, v66, v64
	v_pk_add_f32 v[62:63], s[6:7], v[62:63]
	v_mov_b32_e32 v64, v55
	v_add_f32_e32 v62, v62, v63
	v_fmac_f32_e32 v45, 0xbc800000, v62
	v_mov_b32_dpp v64, v64 row_ror:1 row_mask:0xf bank_mask:0xf
	v_add_f32_e32 v55, v55, v64
	v_mul_f32_e32 v64, v45, v45
	v_readlane_b32 s6, v55, 0
	v_readlane_b32 s8, v55, 16
	v_mov_b32_dpp v64, v64 row_ror:8 row_mask:0xf bank_mask:0xf
	v_fmac_f32_e32 v64, v45, v45
	v_readlane_b32 s7, v55, 32
	v_readlane_b32 s9, v55, 48
	v_mov_b32_e32 v55, v64
	v_mov_b32_e32 v62, s8
	v_mov_b32_e32 v63, s9
	v_mov_b32_dpp v55, v55 row_ror:4 row_mask:0xf bank_mask:0xf
	v_pk_add_f32 v[62:63], s[6:7], v[62:63]
	v_add_f32_e32 v55, v64, v55
	v_mov_b32_e32 v67, v62
	v_mov_b32_e32 v62, v55
	s_nop 1
	v_mov_b32_dpp v62, v62 row_ror:2 row_mask:0xf bank_mask:0xf
	v_add_f32_e32 v55, v55, v62
	v_mov_b32_e32 v62, v55
	s_nop 1
	v_mov_b32_dpp v62, v62 row_ror:1 row_mask:0xf bank_mask:0xf
	v_add_f32_e32 v55, v55, v62
	s_nop 0
	v_readlane_b32 s8, v55, 16
	v_readlane_b32 s9, v55, 48
	v_readlane_b32 s6, v55, 0
	v_readlane_b32 s7, v55, 32
	v_mov_b32_e32 v68, s8
	v_mov_b32_e32 v69, s9
	v_pk_add_f32 v[68:69], s[6:7], v[68:69]
	s_nop 0
	v_mov_b32_e32 v66, v68
	v_mov_b32_e32 v62, v69
	v_pk_add_f32 v[62:63], v[66:67], v[62:63]
	s_nop 0
	v_pk_fma_f32 v[62:63], v[62:63], s[38:39], v[42:43] op_sel_hi:[1,1,0]
	s_nop 0
	v_mul_f32_e32 v55, 0x4b800000, v63
	v_cmp_gt_f32_e64 s[6:7], s11, v63
	v_mul_f32_e32 v64, 0x4b800000, v62
	v_cmp_gt_f32_e64 s[8:9], s11, v62
	v_cndmask_b32_e64 v55, v63, v55, s[6:7]
	v_rsq_f32_e32 v55, v55
	v_cndmask_b32_e64 v62, v62, v64, s[8:9]
	v_rsq_f32_e32 v63, v62
	v_mul_f32_e32 v62, 0x45800000, v55
	v_cndmask_b32_e64 v62, v55, v62, s[6:7]
	v_mul_f32_e32 v64, 0x45800000, v63
	v_cndmask_b32_e64 v55, v63, v64, s[8:9]
	v_pk_mul_f32 v[64:65], v[62:63], v[70:71] op_sel_hi:[0,1]
	v_pk_mul_f32 v[56:57], v[62:63], v[56:57] op_sel_hi:[0,1]
	v_pk_mul_f32 v[66:67], v[62:63], v[72:73] op_sel_hi:[0,1]
	v_pk_mul_f32 v[58:59], v[62:63], v[58:59] op_sel_hi:[0,1]
	v_pk_mul_f32 v[62:63], v[12:13], v[56:57]
	v_pk_mul_f32 v[56:57], v[10:11], v[64:65]
	v_pk_mul_f32 v[64:65], v[4:5], v[58:59]
	v_pk_mul_f32 v[58:59], v[2:3], v[66:67]
	v_mul_f32_e32 v45, v45, v55
	v_cvt_pk_bf16_f32 v56, v56, v57
	v_cvt_pk_bf16_f32 v57, v62, v63
	v_cvt_pk_bf16_f32 v58, v58, v59
	v_cvt_pk_bf16_f32 v59, v64, v65
	v_fma_f32 v45, v43, v45, v48
	global_store_dwordx4 v[60:61], v[56:59], off
	v_cvt_pk_bf16_f32 v45, v45, s0
	s_nop 0
	v_lshl_add_u64 v[56:57], s[30:31], 0, v[28:29]
	global_store_short v[56:57], v45, off
	s_and_saveexec_b64 s[6:7], vcc
	s_cbranch_execz .LBB0_736
	global_load_dword v45, v[46:47], off
	v_readlane_b32 s16, v254, 3
	v_readlane_b32 s30, v254, 17
	v_readlane_b32 s31, v254, 18
	v_readlane_b32 s17, v254, 4
	v_readlane_b32 s18, v254, 5
	v_lshl_add_u64 v[56:57], s[30:31], 0, v[30:31]
	v_readlane_b32 s19, v254, 6
	v_readlane_b32 s20, v254, 7
	v_readlane_b32 s21, v254, 8
	v_readlane_b32 s22, v254, 9
	v_readlane_b32 s23, v254, 10
	v_readlane_b32 s24, v254, 11
	v_readlane_b32 s25, v254, 12
	v_readlane_b32 s26, v254, 13
	v_readlane_b32 s27, v254, 14
	v_readlane_b32 s28, v254, 15
	v_readlane_b32 s29, v254, 16
	s_waitcnt vmcnt(0)
	v_mul_f32_e32 v45, 0x3cb504f3, v45
	global_store_dword v[56:57], v45, off
